# baseline (speedup 1.0000x reference)
_Z8pam_mainPKDv4_jS1_S1_PKfS3_PDF16_Pf:
	s_load_dwordx8 s[4:11], s[0:1], 0x0
	s_load_dwordx4 s[12:15], s[0:1], 0x20
	s_load_dwordx2 s[16:17], s[0:1], 0x30
	v_and_b32_e32 v1, 63, v0
	v_lshrrev_b32_e32 v3, 6, v0
	v_lshlrev_b32_e32 v2, 4, v1
	v_lshlrev_b32_e32 v4, 2, v1
	v_readfirstlane_b32 s18, v3
	v_and_b32_e32 v3, 31, v1
	v_lshlrev_b32_e32 v5, 2, v3
	s_mul_i32 s19, s2, 54
	s_mul_i32 s20, s2, 3
	s_lshr_b32 s20, s20, 4
	s_mul_i32 s21, s20, 0x120
	s_sub_u32 s21, s19, s21
	s_cmp_ge_u32 s20, 24
	s_cselect_b32 s22, 0x120, 0
	s_add_u32 s22, s22, s21
	s_add_u32 s23, s20, 1
	s_cmp_ge_u32 s23, 24
	s_cselect_b32 s24, 0x120, 0
	s_sub_u32 s25, 0x120, s21
	s_cmp_lt_u32 s25, 54
	s_cselect_b32 s26, 1, 0
	s_mul_i32 s25, s25, 43
	s_lshr_b32 s25, s25, 8
	s_cmp_eq_u32 s26, 1
	s_cselect_b32 s25, s25, 100
	s_mov_b32 s29, s2
	s_mov_b32 s46, 0
	s_mov_b32 s47, 30720
	s_mov_b32 s48, 61440
	s_mov_b32 s27, 0
	s_mov_b32 s28, 1
	s_mul_i32 s30, s18, 0xd00
	s_add_u32 s30, s30, 92160
	v_add_u32_e32 v7, s30, v2
	v_mul_u32_u24_e32 v6, 0x68, v3
	v_lshrrev_b32_e32 v130, 2, v1
	v_and_b32_e32 v130, 8, v130
	v_add3_u32 v6, v6, v130, s30
	v_mov_b32_e32 v150, 0xf149f2ca
	s_waitcnt lgkmcnt(0)
	s_lshl_b32 s33, s18, 10
	s_lshl_b32 s30, s22, 12
	s_add_u32 s30, s30, s33
	s_add_u32 s50, s8, s30
	s_addc_u32 s51, s9, 0
	s_lshl_b32 s30, s22, 10
	s_add_u32 s30, s30, s33
	s_add_u32 s54, s4, s30
	s_addc_u32 s55, s5, 0
	s_lshl_b32 s30, s24, 12
	s_add_u32 s30, s30, s33
	s_add_u32 s64, s8, s30
	s_addc_u32 s65, s9, 0
	s_lshl_b32 s30, s24, 10
	s_add_u32 s30, s30, s33
	s_add_u32 s66, s4, s30
	s_addc_u32 s67, s5, 0
	s_cmp_eq_u32 s27, s25
	s_cbranch_scc0 .Lm_ns_p0
	s_mov_b64 s[50:51], s[64:65]
	s_mov_b64 s[54:55], s[66:67]
.Lm_ns_p0:
	s_add_u32 s34, s46, s33
	s_mov_b32 m0, s34
	s_add_u32 s52, s50, 0x3000
	s_addc_u32 s53, s51, 0
	global_load_lds_dwordx4 v2, s[50:51]
	s_add_u32 s35, s34, 0x3000
	s_mov_b32 m0, s35
	s_add_u32 s36, s34, 24576
	global_load_lds_dwordx4 v2, s[52:53]
	s_cmp_lt_u32 s18, 6
	s_cbranch_scc0 .Lm_nok_p0
	s_mov_b32 m0, s36
	s_nop 0
	global_load_lds_dwordx4 v2, s[54:55]
.Lm_nok_p0:
	s_add_u32 s50, s50, 0x6000
	s_addc_u32 s51, s51, 0
	s_add_u32 s54, s54, 0x1800
	s_addc_u32 s55, s55, 0
	global_load_dwordx4 v[132:135], v2, s[12:13]
	global_load_dwordx4 v[136:139], v2, s[12:13] offset:1024
	global_load_dword v140, v4, s[12:13] offset:2048
	s_mul_i32 s30, s20, 12
	s_add_u32 s30, s30, s18
	s_add_u32 s31, s20, s26
	s_mul_i32 s31, s31, 12
	s_add_u32 s31, s31, s18
	s_lshl_b32 s36, s30, 10
	s_add_u32 s56, s6, s36
	s_addc_u32 s57, s7, 0
	s_lshl_b32 s36, s31, 10
	s_add_u32 s58, s6, s36
	s_addc_u32 s59, s7, 0
	global_load_dwordx4 v[8:11], v2, s[56:57]
	global_load_dwordx4 v[12:15], v2, s[58:59]
	s_lshl_b32 s36, s30, 7
	s_add_u32 s60, s10, s36
	s_addc_u32 s61, s11, 0
	s_lshl_b32 s36, s31, 7
	s_add_u32 s62, s10, s36
	s_addc_u32 s63, s11, 0
	global_load_dword v141, v5, s[60:61]
	global_load_dword v142, v5, s[62:63]
	s_cmp_eq_u32 s28, s25
	s_cbranch_scc0 .Lm_ns_p1
	s_mov_b64 s[50:51], s[64:65]
	s_mov_b64 s[54:55], s[66:67]
.Lm_ns_p1:
	s_add_u32 s34, s47, s33
	s_mov_b32 m0, s34
	s_add_u32 s52, s50, 0x3000
	s_addc_u32 s53, s51, 0
	global_load_lds_dwordx4 v2, s[50:51]
	s_add_u32 s35, s34, 0x3000
	s_mov_b32 m0, s35
	s_add_u32 s36, s34, 24576
	global_load_lds_dwordx4 v2, s[52:53]
	s_cmp_lt_u32 s18, 6
	s_cbranch_scc0 .Lm_nok_p1
	s_mov_b32 m0, s36
	s_nop 0
	global_load_lds_dwordx4 v2, s[54:55]
.Lm_nok_p1:
	s_add_u32 s50, s50, 0x6000
	s_addc_u32 s51, s51, 0
	s_add_u32 s54, s54, 0x1800
	s_addc_u32 s55, s55, 0
	s_waitcnt vmcnt(2)
	s_nop 0
	v_max3_f32 v132, v132, v133, v134
	v_max3_f32 v136, v136, v137, v138
	v_max3_f32 v132, v132, v135, v139
	v_max3_f32 v132, v132, v136, v140
	s_nop 1
	v_max_f32_dpp v132, v132, v132 quad_perm:[1,0,3,2] row_mask:0xf bank_mask:0xf
	s_nop 1
	v_max_f32_dpp v132, v132, v132 quad_perm:[2,3,0,1] row_mask:0xf bank_mask:0xf
	s_nop 1
	v_max_f32_dpp v132, v132, v132 row_half_mirror row_mask:0xf bank_mask:0xf
	s_nop 1
	v_max_f32_dpp v132, v132, v132 row_mirror row_mask:0xf bank_mask:0xf
	s_nop 1
	v_readlane_b32 s36, v132, 0
	v_readlane_b32 s37, v132, 16
	v_readlane_b32 s38, v132, 32
	v_readlane_b32 s39, v132, 48
	s_nop 2
	v_mov_b32_e32 v133, s36
	v_max_f32_e32 v133, s37, v133
	v_max_f32_e32 v133, s38, v133
	v_max_f32_e32 v133, s39, v133
	s_mov_b32 s37, 0xf800000
	v_mul_f32_e32 v137, 0x4f800000, v133
	v_cmp_gt_f32_e32 vcc, s37, v133
	s_nop 1
	v_cndmask_b32_e32 v133, v133, v137, vcc
	v_sqrt_f32_e32 v137, v133
	s_nop 0
	v_add_u32_e32 v138, -1, v137
	v_add_u32_e32 v139, 1, v137
	v_fma_f32 v143, -v138, v137, v133
	v_fma_f32 v144, -v139, v137, v133
	v_cmp_ge_f32_e64 s[38:39], 0, v143
	s_nop 1
	v_cndmask_b32_e64 v137, v137, v138, s[38:39]
	v_cmp_lt_f32_e64 s[38:39], 0, v144
	s_nop 1
	v_cndmask_b32_e64 v137, v137, v139, s[38:39]
	v_mul_f32_e32 v138, 0x37800000, v137
	v_cndmask_b32_e32 v137, v137, v138, vcc
	v_mov_b32_e32 v138, 0x260
	v_cmp_class_f32_e32 vcc, v133, v138
	s_nop 1
	v_cndmask_b32_e32 v133, v137, v133, vcc
	v_mov_b32_e32 v135, 0x3ca3d70a
	s_mov_b32 s36, 0xffff
	v_mul_f32_e32 v134, v141, v133
	v_mul_f32_e32 v136, v142, v133
	v_fmamk_f32 v134, v134, 0x3f804189, v135
	v_fmamk_f32 v136, v136, 0x3f804189, v135
	v_cvt_f16_f32_e64 v134, -v134
	v_cvt_f16_f32_e64 v136, -v136
	v_cmp_gt_u32_e32 vcc, 32, v1
	v_cvt_f32_f16_e32 v148, v134
	v_cvt_f32_f16_e32 v149, v136
	v_bfi_b32 v134, s36, v134, v11
	v_bfi_b32 v136, s36, v136, v15
	v_cndmask_b32_e32 v11, v11, v134, vcc
	v_cndmask_b32_e32 v15, v15, v136, vcc
	s_waitcnt vmcnt(0)
	s_barrier
	s_mov_b32 s28, 2
	v_add_u32_e32 v128, s46, v2
	v_add_u32_e32 v129, s47, v2
	ds_read_b128 v[88:91], v128 offset:24576
	ds_read_b128 v[92:95], v128 offset:25600
	ds_read_b128 v[96:99], v128 offset:0
	ds_read_b128 v[104:107], v128 offset:2048
	ds_read_b128 v[100:103], v128 offset:1024
	ds_read_b128 v[108:111], v128 offset:3072
	s_cmp_eq_u32 s28, s25
	s_cbranch_scc0 .Lm_ns_p2
	s_mov_b64 s[50:51], s[64:65]
	s_mov_b64 s[54:55], s[66:67]
.Lm_ns_p2:
	s_add_u32 s34, s48, s33
	s_mov_b32 m0, s34
	s_add_u32 s52, s50, 0x3000
	s_addc_u32 s53, s51, 0
	global_load_lds_dwordx4 v2, s[50:51]
	s_add_u32 s35, s34, 0x3000
	s_mov_b32 m0, s35
	s_add_u32 s36, s34, 24576
	global_load_lds_dwordx4 v2, s[52:53]
	s_cmp_lt_u32 s18, 6
	s_cbranch_scc0 .Lm_nok_p2
	s_mov_b32 m0, s36
	s_nop 0
	global_load_lds_dwordx4 v2, s[54:55]
.Lm_nok_p2:
	s_add_u32 s50, s50, 0x6000
	s_addc_u32 s51, s51, 0
	s_add_u32 s54, s54, 0x1800
	s_addc_u32 s55, s55, 0
	s_waitcnt lgkmcnt(5)
	v_mfma_f32_32x32x16_f16 v[48:63], v[88:91], v[8:11], 0
	s_nop 5
	s_waitcnt lgkmcnt(4)
	v_mfma_f32_32x32x16_f16 v[64:79], v[92:95], v[8:11], 0
	ds_read_b128 v[88:91], v128 offset:26624
	ds_read_b128 v[112:115], v128 offset:4096
	ds_read_b128 v[120:123], v128 offset:6144
	v_exp_f32_e32 v48, v48
	v_exp_f32_e32 v49, v49
	v_exp_f32_e32 v50, v50
	v_exp_f32_e32 v51, v51
	v_exp_f32_e32 v52, v52
	v_exp_f32_e32 v53, v53
	v_exp_f32_e32 v54, v54
	v_exp_f32_e32 v55, v55
	v_cvt_pk_bf16_f32 v80, v48, v49
	v_cvt_pk_bf16_f32 v81, v50, v51
	v_cvt_pk_bf16_f32 v82, v52, v53
	v_cvt_pk_bf16_f32 v83, v54, v55
	ds_read_b128 v[116:119], v128 offset:5120
	ds_read_b128 v[124:127], v128 offset:7168
	v_exp_f32_e32 v56, v56
	v_exp_f32_e32 v57, v57
	v_exp_f32_e32 v58, v58
	v_exp_f32_e32 v59, v59
	s_waitcnt lgkmcnt(7)
	v_mfma_f32_32x32x16_bf16 v[16:31], v[96:99], v[80:83], 0
	v_exp_f32_e32 v60, v60
	v_exp_f32_e32 v61, v61
	v_exp_f32_e32 v62, v62
	v_exp_f32_e32 v63, v63
	v_mfma_f32_32x32x16_bf16 v[32:47], v[104:107], v[80:83], 0
	v_cvt_pk_bf16_f32 v84, v56, v57
	v_cvt_pk_bf16_f32 v85, v58, v59
	v_cvt_pk_bf16_f32 v86, v60, v61
	v_cvt_pk_bf16_f32 v87, v62, v63
	s_branch .Lm_steps1
.Lm_steps:
	s_waitcnt lgkmcnt(4)
	v_mfma_f32_32x32x16_f16 v[64:79], v[92:95], v[8:11], 0
	ds_read_b128 v[88:91], v128 offset:26624
	ds_read_b128 v[112:115], v128 offset:4096
	ds_read_b128 v[120:123], v128 offset:6144
	v_exp_f32_e32 v48, v48
	v_exp_f32_e32 v49, v49
	v_exp_f32_e32 v50, v50
	v_exp_f32_e32 v51, v51
	v_exp_f32_e32 v52, v52
	v_exp_f32_e32 v53, v53
	v_exp_f32_e32 v54, v54
	v_exp_f32_e32 v55, v55
	v_cvt_pk_bf16_f32 v80, v48, v49
	v_cvt_pk_bf16_f32 v81, v50, v51
	v_cvt_pk_bf16_f32 v82, v52, v53
	v_cvt_pk_bf16_f32 v83, v54, v55
	ds_read_b128 v[116:119], v128 offset:5120
	ds_read_b128 v[124:127], v128 offset:7168
	v_exp_f32_e32 v56, v56
	v_exp_f32_e32 v57, v57
	v_exp_f32_e32 v58, v58
	v_exp_f32_e32 v59, v59
	s_waitcnt lgkmcnt(7)
	v_mfma_f32_32x32x16_bf16 v[16:31], v[96:99], v[80:83], v[16:31]
	v_exp_f32_e32 v60, v60
	v_exp_f32_e32 v61, v61
	v_exp_f32_e32 v62, v62
	v_exp_f32_e32 v63, v63
	v_mfma_f32_32x32x16_bf16 v[32:47], v[104:107], v[80:83], v[32:47]
	v_cvt_pk_bf16_f32 v84, v56, v57
	v_cvt_pk_bf16_f32 v85, v58, v59
	v_cvt_pk_bf16_f32 v86, v60, v61
	v_cvt_pk_bf16_f32 v87, v62, v63
	s_cmp_lt_u32 s28, 9
	s_cbranch_scc0 .Lm_nod_lp
	s_cmp_eq_u32 s28, s25
	s_cbranch_scc0 .Lm_ns_lp
	s_mov_b64 s[50:51], s[64:65]
	s_mov_b64 s[54:55], s[66:67]

.Lm_nok_lp:
	s_add_u32 s50, s50, 0x6000
	s_addc_u32 s51, s51, 0
	s_add_u32 s54, s54, 0x1800
	s_addc_u32 s55, s55, 0
